# baseline with only the 16 P6 gate loads marked non-temporal
# speedup vs baseline: 1.0158x; 1.0058x over previous
; __device__ __forceinline__ void unpack8(const v4u w, float (&o)[8]) { o[0] = bflo(w.x); o[1] = bfhi(w.x); o[2] = bflo(w.y); o[3] = bfhi(w.y); o[4] = bflo(w.z); o[5] = bfhi(w.z); o[6] = bflo(w.w); o[7] = bfhi(w.w); }
; __device__ __forceinline__ v4u pack8(const float (&o)[8]) { v4u w; w.x = pk2(o[0], o[1]); w.y = pk2(o[2], o[3]); w.z = pk2(o[4], o[5]); w.w = pk2(o[6], o[7]); return w; }
; __device__ __forceinline__ float sigmf(float x) { return __builtin_amdgcn_rcpf(1.f + __expf(-x)); }
;     __device__ __forceinline__ void operator()(const f32x4 (&acc)[2][2][4][2], const pg8::Unit& u, int wr, int wc, int fr, int fq_in) const {
;     ...
;         const int row0 = u.pm * 256 + wr * 64 + fr, col0 = u.pn * 256 + wc * 32 + 8 * fq; const bool first = u.sel == 0; const int goff = first ? 0 : D;
; #pragma unroll
;         for (int bj = 0; bj < 2; ++bj) {
;             const int col = col0 + bj * 128;
;             float b0[8];
;             { const f32x4 t0 = *(const f32x4*)(bg + goff + col), t1 = *(const f32x4*)(bg + goff + col + 4);
; #pragma unroll
;               for (int q = 0; q < 4; ++q) { b0[q] = t0[q]; b0[4 + q] = t1[q]; } }
; #pragma unroll
;             for (int ai = 0; ai < 2; ++ai) {
;                 v4u gw_[4], pw_[4];
; #pragma unroll
;                 for (int m = 0; m < 4; ++m) { const size_t row = (size_t)(row0 + ai * 128 + m * 16);
;                     gw_[m] = *(const v4u*)(Gt + row * (2 * D) + goff + col); pw_[m] = first ? (v4u){0u, 0u, 0u, 0u} : *(const v4u*)(O + row * D + col); }
;                 __builtin_amdgcn_sched_barrier(0);
; #pragma unroll
;                 for (int m = 0; m < 4; ++m) { const size_t row = (size_t)(row0 + ai * 128 + m * 16);
;                     float g0[8], p[8]; unpack8(gw_[m], g0); unpack8(pw_[m], p);
;                     float o[8];
; #pragma unroll
;                     for (int q = 0; q < 4; ++q) { o[q] = p[q] + sigmf(g0[q] + b0[q]) * acc[ai][bj][m][0][q]; o[4 + q] = p[4 + q] + sigmf(g0[4 + q] + b0[4 + q]) * acc[ai][bj][m][1][q]; }
;                     *(v4u*)(O + row * D + col) = pack8(o); }
.LBB0_903:
	s_lshl_b32 s17, s26, 8
	s_and_b64 s[8:9], s[30:31], exec
	v_mov_b32_e32 v114, v1
	s_cselect_b32 s19, 0x800, 0
	s_or_b32 s8, s17, s50
	v_lshl_add_u32 v202, s28, 8, v216
	v_lshl_add_u32 v138, v114, 3, s8
	s_lshl_b32 s8, s19, 2
	s_add_u32 s8, s0, s8
	s_addc_u32 s9, s1, 0
	v_ashrrev_i32_e32 v139, 31, v138
	v_lshl_add_u64 v[190:191], v[138:139], 2, s[8:9]
	s_lshl_b32 s8, s19, 1
	s_add_u32 s8, s48, s8
	s_addc_u32 s9, s49, 0
	v_lshlrev_b64 v[192:193], 1, v[138:139]
	v_ashrrev_i32_e32 v203, 31, v202
	v_lshl_add_u64 v[206:207], s[8:9], 0, v[192:193]
	v_lshlrev_b64 v[138:139], 13, v[202:203]
	v_lshl_add_u64 v[194:195], v[206:207], 0, v[138:139]
	global_load_dwordx4 v[114:117], v[190:191], off offset:16
	global_load_dwordx4 v[118:121], v[190:191], off
	global_load_dwordx4 v[168:171], v[194:195], off nt
	v_cndmask_b32_e64 v138, 0, 1, s[30:31]
	v_lshl_add_u64 v[204:205], s[4:5], 0, v[192:193]
	v_mov_b32_e32 v144, 0
	v_cmp_ne_u32_e64 s[8:9], 1, v138
	s_andn2_b64 vcc, exec, s[30:31]
	v_lshlrev_b64 v[214:215], 12, v[202:203]
	v_mov_b32_e32 v164, 0
	v_mov_b32_e32 v165, 0
	v_mov_b32_e32 v166, 0
	v_mov_b32_e32 v167, 0
	s_cbranch_vccnz .LBB0_905
	v_lshl_add_u64 v[138:139], v[204:205], 0, v[214:215]
	global_load_dwordx4 v[164:167], v[138:139], off
.LBB0_905:
	v_or_b32_e32 v138, 16, v202
	v_ashrrev_i32_e32 v139, 31, v138
	v_lshlrev_b64 v[140:141], 13, v[138:139]
	v_lshl_add_u64 v[196:197], v[206:207], 0, v[140:141]
	global_load_dwordx4 v[160:163], v[196:197], off nt
	s_and_b64 vcc, exec, s[8:9]
	v_lshlrev_b64 v[212:213], 12, v[138:139]
	v_mov_b32_e32 v156, 0
	v_mov_b32_e32 v157, 0
	v_mov_b32_e32 v158, 0
	v_mov_b32_e32 v159, 0
	s_cbranch_vccnz .LBB0_907
	v_lshl_add_u64 v[138:139], v[204:205], 0, v[212:213]
	global_load_dwordx4 v[156:159], v[138:139], off
.LBB0_907:
	v_or_b32_e32 v138, 32, v202
	v_ashrrev_i32_e32 v139, 31, v138
	v_lshlrev_b64 v[140:141], 13, v[138:139]
	v_lshl_add_u64 v[198:199], v[206:207], 0, v[140:141]
	global_load_dwordx4 v[152:155], v[198:199], off nt
	s_and_b64 vcc, exec, s[8:9]
	v_lshlrev_b64 v[210:211], 12, v[138:139]
	v_mov_b32_e32 v145, 0
	v_mov_b32_e32 v146, 0
	v_mov_b32_e32 v147, 0
	s_cbranch_vccnz .LBB0_909
	v_lshl_add_u64 v[138:139], v[204:205], 0, v[210:211]
	global_load_dwordx4 v[144:147], v[138:139], off
.LBB0_909:
	v_or_b32_e32 v138, 48, v202
	v_ashrrev_i32_e32 v139, 31, v138
	v_lshlrev_b64 v[140:141], 13, v[138:139]
	v_lshl_add_u64 v[200:201], v[206:207], 0, v[140:141]
	global_load_dwordx4 v[148:151], v[200:201], off nt
	v_lshlrev_b64 v[208:209], 12, v[138:139]
	v_mov_b32_e32 v138, 0
	s_and_b64 vcc, exec, s[8:9]
	v_mov_b32_e32 v140, 0
	v_mov_b32_e32 v141, 0
	v_mov_b32_e32 v142, 0
	v_mov_b32_e32 v143, 0
	s_cbranch_vccnz .LBB0_911
	v_lshl_add_u64 v[140:141], v[204:205], 0, v[208:209]
	global_load_dwordx4 v[140:143], v[140:141], off
.LBB0_911:
	s_waitcnt vmcnt(0)
	v_lshlrev_b32_e32 v139, 16, v168
	v_lshlrev_b32_e32 v203, 16, v169
	v_and_b32_e32 v221, 0xffff0000, v169
	v_lshlrev_b32_e32 v169, 16, v170
	v_add_f32_e32 v139, v118, v139
	v_and_b32_e32 v168, 0xffff0000, v168
	v_mul_f32_e32 v139, 0xbfb8aa3b, v139
	v_add_f32_e32 v169, v114, v169
	v_exp_f32_e32 v139, v139
	v_mul_f32_e32 v169, 0xbfb8aa3b, v169
	v_add_f32_e32 v168, v119, v168
	v_exp_f32_e32 v169, v169
	v_mul_f32_e32 v168, 0xbfb8aa3b, v168
	v_lshlrev_b32_e32 v224, 16, v171
	v_and_b32_e32 v225, 0xffff0000, v171
	v_exp_f32_e32 v171, v168
	v_add_f32_e32 v139, 1.0, v139
	v_rcp_f32_e32 v168, v139
	v_add_f32_e32 v139, 1.0, v169
	v_and_b32_e32 v222, 0xffff0000, v170
	v_rcp_f32_e32 v170, v139
	v_add_f32_e32 v139, 1.0, v171
	v_rcp_f32_e32 v169, v139
	v_add_f32_e32 v139, v115, v222
	v_mul_f32_e32 v139, 0xbfb8aa3b, v139
	v_exp_f32_e32 v139, v139
	v_lshlrev_b32_e32 v222, 16, v164
	v_and_b32_e32 v223, 0xffff0000, v164
	v_pk_fma_f32 v[134:135], v[134:135], v[168:169], v[222:223]
	v_add_f32_e32 v139, 1.0, v139
	v_rcp_f32_e32 v171, v139
	v_add_f32_e32 v139, v120, v203
	v_mul_f32_e32 v139, 0xbfb8aa3b, v139
	v_exp_f32_e32 v139, v139
	v_lshlrev_b32_e32 v168, 16, v166
	v_and_b32_e32 v169, 0xffff0000, v166
	v_pk_fma_f32 v[168:169], v[130:131], v[170:171], v[168:169]
	v_add_f32_e32 v131, v116, v224
	v_add_f32_e32 v130, 1.0, v139
	v_mul_f32_e32 v131, 0xbfb8aa3b, v131
	v_add_f32_e32 v139, v121, v221
	v_exp_f32_e32 v131, v131
	v_mul_f32_e32 v139, 0xbfb8aa3b, v139
	v_exp_f32_e32 v139, v139
	v_rcp_f32_e32 v130, v130
	v_add_f32_e32 v131, 1.0, v131
	v_rcp_f32_e32 v164, v131
	v_add_f32_e32 v131, 1.0, v139
	v_add_f32_e32 v139, v117, v225
	v_mul_f32_e32 v139, 0xbfb8aa3b, v139
	v_exp_f32_e32 v139, v139
	v_rcp_f32_e32 v131, v131
	v_lshlrev_b32_e32 v170, 16, v165
	v_and_b32_e32 v171, 0xffff0000, v165
	v_add_f32_e32 v139, 1.0, v139
	v_rcp_f32_e32 v165, v139
	v_pk_fma_f32 v[136:137], v[136:137], v[130:131], v[170:171]
	v_lshlrev_b32_e32 v130, 16, v167
	v_and_b32_e32 v131, 0xffff0000, v167
	v_pk_fma_f32 v[164:165], v[132:133], v[164:165], v[130:131]
	v_cvt_pk_bf16_f32 v130, v134, v135
	v_lshl_add_u64 v[134:135], s[4:5], 0, v[214:215]
	v_cvt_pk_bf16_f32 v131, v136, v137
	v_cvt_pk_bf16_f32 v132, v168, v169
	v_cvt_pk_bf16_f32 v133, v164, v165
	v_lshl_add_u64 v[164:165], v[134:135], 0, v[192:193]
	global_store_dwordx4 v[164:165], v[130:133], off
	v_lshlrev_b32_e32 v134, 16, v156
	v_and_b32_e32 v135, 0xffff0000, v156
	v_lshlrev_b32_e32 v130, 16, v160
	v_and_b32_e32 v131, 0xffff0000, v160
	v_add_f32_e32 v130, v118, v130
	v_add_f32_e32 v131, v119, v131
	v_mul_f32_e32 v130, 0xbfb8aa3b, v130
	v_mul_f32_e32 v131, 0xbfb8aa3b, v131
	v_exp_f32_e32 v130, v130
	v_exp_f32_e32 v131, v131
	v_lshlrev_b32_e32 v132, 16, v162
	v_and_b32_e32 v133, 0xffff0000, v162
	v_add_f32_e32 v132, v114, v132
	v_add_f32_e32 v133, v115, v133
; __device__ __forceinline__ void unpack8(const v4u w, float (&o)[8]) { o[0] = bflo(w.x); o[1] = bfhi(w.x); o[2] = bflo(w.y); o[3] = bfhi(w.y); o[4] = bflo(w.z); o[5] = bfhi(w.z); o[6] = bflo(w.w); o[7] = bfhi(w.w); }
; __device__ __forceinline__ v4u pack8(const float (&o)[8]) { v4u w; w.x = pk2(o[0], o[1]); w.y = pk2(o[2], o[3]); w.z = pk2(o[4], o[5]); w.w = pk2(o[6], o[7]); return w; }
; __device__ __forceinline__ float sigmf(float x) { return __builtin_amdgcn_rcpf(1.f + __expf(-x)); }
;     __device__ __forceinline__ void operator()(const f32x4 (&acc)[2][2][4][2], const pg8::Unit& u, int wr, int wc, int fr, int fq_in) const {
;     ...
;                 for (int m = 0; m < 4; ++m) { const size_t row = (size_t)(row0 + ai * 128 + m * 16);
;                     gw_[m] = *(const v4u*)(Gt + row * (2 * D) + goff + col); pw_[m] = first ? (v4u){0u, 0u, 0u, 0u} : *(const v4u*)(O + row * D + col); }
;                 __builtin_amdgcn_sched_barrier(0);
; #pragma unroll
;                 for (int m = 0; m < 4; ++m) { const size_t row = (size_t)(row0 + ai * 128 + m * 16);
;                     float g0[8], p[8]; unpack8(gw_[m], g0); unpack8(pw_[m], p);
;                     float o[8];
; #pragma unroll
;                     for (int q = 0; q < 4; ++q) { o[q] = p[q] + sigmf(g0[q] + b0[q]) * acc[ai][bj][m][0][q]; o[4 + q] = p[4 + q] + sigmf(g0[4 + q] + b0[4 + q]) * acc[ai][bj][m][1][q]; }
;                     *(v4u*)(O + row * D + col) = pack8(o); }
	v_add_f32_e32 v130, 1.0, v130
	v_mul_f32_e32 v132, 0xbfb8aa3b, v132
	v_add_f32_e32 v131, 1.0, v131
	v_mul_f32_e32 v133, 0xbfb8aa3b, v133
	v_exp_f32_e32 v132, v132
	v_rcp_f32_e32 v130, v130
	v_rcp_f32_e32 v131, v131
	v_exp_f32_e32 v133, v133
	v_add_f32_e32 v132, 1.0, v132
	v_lshlrev_b32_e32 v136, 16, v161
	v_pk_fma_f32 v[126:127], v[126:127], v[130:131], v[134:135]
	v_add_f32_e32 v130, 1.0, v133
	v_rcp_f32_e32 v132, v132
	v_rcp_f32_e32 v133, v130
	v_add_f32_e32 v130, v120, v136
	v_mul_f32_e32 v130, 0xbfb8aa3b, v130
	v_lshlrev_b32_e32 v139, 16, v163
	v_exp_f32_e32 v134, v130
	v_lshlrev_b32_e32 v130, 16, v158
	v_and_b32_e32 v131, 0xffff0000, v158
	v_and_b32_e32 v137, 0xffff0000, v161
	v_pk_fma_f32 v[130:131], v[122:123], v[132:133], v[130:131]
	v_add_f32_e32 v123, v116, v139
	v_mul_f32_e32 v123, 0xbfb8aa3b, v123
	v_add_f32_e32 v132, v121, v137
	v_exp_f32_e32 v123, v123
	v_mul_f32_e32 v132, 0xbfb8aa3b, v132
	v_exp_f32_e32 v133, v132
	v_and_b32_e32 v160, 0xffff0000, v163
	v_add_f32_e32 v123, 1.0, v123
	v_rcp_f32_e32 v132, v123
	v_add_f32_e32 v123, 1.0, v133
	v_add_f32_e32 v133, v117, v160
	v_mul_f32_e32 v133, 0xbfb8aa3b, v133
	v_exp_f32_e32 v133, v133
	v_add_f32_e32 v122, 1.0, v134
	v_rcp_f32_e32 v122, v122
	v_rcp_f32_e32 v123, v123
	v_add_f32_e32 v133, 1.0, v133
	v_rcp_f32_e32 v133, v133
	v_lshlrev_b32_e32 v134, 16, v157
	v_and_b32_e32 v135, 0xffff0000, v157
	v_pk_fma_f32 v[128:129], v[128:129], v[122:123], v[134:135]
	v_lshlrev_b32_e32 v122, 16, v159
	v_and_b32_e32 v123, 0xffff0000, v159
	v_pk_fma_f32 v[132:133], v[124:125], v[132:133], v[122:123]
	v_cvt_pk_bf16_f32 v122, v126, v127
	v_lshl_add_u64 v[126:127], s[4:5], 0, v[212:213]
	v_cvt_pk_bf16_f32 v123, v128, v129
	v_cvt_pk_bf16_f32 v124, v130, v131
	v_cvt_pk_bf16_f32 v125, v132, v133
	v_lshl_add_u64 v[156:157], v[126:127], 0, v[192:193]
	global_store_dwordx4 v[156:157], v[122:125], off
	v_lshlrev_b32_e32 v126, 16, v144
	v_and_b32_e32 v127, 0xffff0000, v144
	v_lshlrev_b32_e32 v122, 16, v152
	v_and_b32_e32 v123, 0xffff0000, v152
	v_add_f32_e32 v122, v118, v122
	v_add_f32_e32 v123, v119, v123
	v_mul_f32_e32 v122, 0xbfb8aa3b, v122
	v_mul_f32_e32 v123, 0xbfb8aa3b, v123
	v_exp_f32_e32 v122, v122
	v_exp_f32_e32 v123, v123
	v_lshlrev_b32_e32 v124, 16, v154
	v_and_b32_e32 v125, 0xffff0000, v154
	v_add_f32_e32 v124, v114, v124
	v_add_f32_e32 v125, v115, v125
	v_add_f32_e32 v122, 1.0, v122
	v_mul_f32_e32 v124, 0xbfb8aa3b, v124
	v_add_f32_e32 v123, 1.0, v123
	v_mul_f32_e32 v125, 0xbfb8aa3b, v125
	v_exp_f32_e32 v124, v124
	v_rcp_f32_e32 v122, v122
	v_rcp_f32_e32 v123, v123
	v_exp_f32_e32 v125, v125
	v_add_f32_e32 v124, 1.0, v124
	v_lshlrev_b32_e32 v128, 16, v153
	v_pk_fma_f32 v[110:111], v[110:111], v[122:123], v[126:127]
	v_add_f32_e32 v122, 1.0, v125
	v_rcp_f32_e32 v124, v124
	v_rcp_f32_e32 v125, v122
	v_add_f32_e32 v122, v120, v128
	v_mul_f32_e32 v122, 0xbfb8aa3b, v122
	v_lshlrev_b32_e32 v130, 16, v155
	v_exp_f32_e32 v126, v122
	v_lshlrev_b32_e32 v122, 16, v146
	v_and_b32_e32 v123, 0xffff0000, v146
	v_and_b32_e32 v129, 0xffff0000, v153
	v_pk_fma_f32 v[122:123], v[106:107], v[124:125], v[122:123]
	v_add_f32_e32 v107, v116, v130
	v_mul_f32_e32 v107, 0xbfb8aa3b, v107
	v_add_f32_e32 v124, v121, v129
	v_exp_f32_e32 v107, v107
	v_mul_f32_e32 v124, 0xbfb8aa3b, v124
	v_exp_f32_e32 v125, v124
	v_and_b32_e32 v131, 0xffff0000, v155
	v_add_f32_e32 v107, 1.0, v107
	v_rcp_f32_e32 v124, v107
	v_add_f32_e32 v107, 1.0, v125
	v_add_f32_e32 v125, v117, v131
	v_mul_f32_e32 v125, 0xbfb8aa3b, v125
	v_exp_f32_e32 v125, v125
	v_add_f32_e32 v106, 1.0, v126
	v_rcp_f32_e32 v106, v106
	v_rcp_f32_e32 v107, v107
	v_add_f32_e32 v125, 1.0, v125
	v_rcp_f32_e32 v125, v125
	v_lshlrev_b32_e32 v126, 16, v145
	v_and_b32_e32 v127, 0xffff0000, v145
	v_pk_fma_f32 v[112:113], v[112:113], v[106:107], v[126:127]
	v_lshlrev_b32_e32 v106, 16, v147
	v_and_b32_e32 v107, 0xffff0000, v147
	v_pk_fma_f32 v[124:125], v[108:109], v[124:125], v[106:107]
	v_cvt_pk_bf16_f32 v106, v110, v111
	v_lshl_add_u64 v[110:111], s[4:5], 0, v[210:211]
	v_cvt_pk_bf16_f32 v107, v112, v113
	v_cvt_pk_bf16_f32 v108, v122, v123
	v_cvt_pk_bf16_f32 v109, v124, v125
	v_lshl_add_u64 v[112:113], v[110:111], 0, v[192:193]
	global_store_dwordx4 v[112:113], v[106:109], off
	v_lshlrev_b32_e32 v110, 16, v140
	v_and_b32_e32 v111, 0xffff0000, v140
	v_lshlrev_b32_e32 v106, 16, v148
	v_and_b32_e32 v107, 0xffff0000, v148
	v_add_f32_e32 v106, v118, v106
	v_add_f32_e32 v107, v119, v107
	v_mul_f32_e32 v106, 0xbfb8aa3b, v106
	v_mul_f32_e32 v107, 0xbfb8aa3b, v107
	v_exp_f32_e32 v106, v106
	v_exp_f32_e32 v107, v107
	v_lshlrev_b32_e32 v108, 16, v150
	v_and_b32_e32 v109, 0xffff0000, v150
	v_add_f32_e32 v108, v114, v108
	v_add_f32_e32 v109, v115, v109
	v_add_f32_e32 v106, 1.0, v106
	v_mul_f32_e32 v108, 0xbfb8aa3b, v108
	v_add_f32_e32 v107, 1.0, v107
	v_mul_f32_e32 v109, 0xbfb8aa3b, v109
	v_exp_f32_e32 v108, v108
	v_rcp_f32_e32 v106, v106
	v_rcp_f32_e32 v107, v107
	v_exp_f32_e32 v109, v109
	v_add_f32_e32 v108, 1.0, v108
	v_lshlrev_b32_e32 v122, 16, v149
	v_pk_fma_f32 v[102:103], v[102:103], v[106:107], v[110:111]
	v_add_f32_e32 v106, 1.0, v109
	v_rcp_f32_e32 v108, v108
	v_rcp_f32_e32 v109, v106
	v_add_f32_e32 v106, v120, v122
	v_mul_f32_e32 v106, 0xbfb8aa3b, v106
	v_lshlrev_b32_e32 v124, 16, v151
	v_exp_f32_e32 v110, v106
	v_lshlrev_b32_e32 v106, 16, v142
	v_and_b32_e32 v107, 0xffff0000, v142
	v_and_b32_e32 v123, 0xffff0000, v149
	v_pk_fma_f32 v[106:107], v[98:99], v[108:109], v[106:107]
	v_add_f32_e32 v99, v116, v124
	v_mul_f32_e32 v99, 0xbfb8aa3b, v99
	v_add_f32_e32 v108, v121, v123
	v_exp_f32_e32 v99, v99
	v_mul_f32_e32 v108, 0xbfb8aa3b, v108
	v_exp_f32_e32 v109, v108
	v_and_b32_e32 v125, 0xffff0000, v151
	v_add_f32_e32 v99, 1.0, v99
	v_rcp_f32_e32 v108, v99
	v_add_f32_e32 v99, 1.0, v109
	v_add_f32_e32 v109, v117, v125
	v_mul_f32_e32 v109, 0xbfb8aa3b, v109
	v_exp_f32_e32 v109, v109
	v_add_f32_e32 v98, 1.0, v110
	v_rcp_f32_e32 v98, v98
	v_rcp_f32_e32 v99, v99
	v_add_f32_e32 v109, 1.0, v109
	v_rcp_f32_e32 v109, v109
	v_lshlrev_b32_e32 v110, 16, v141
	v_and_b32_e32 v111, 0xffff0000, v141
	v_pk_fma_f32 v[104:105], v[104:105], v[98:99], v[110:111]
	v_lshlrev_b32_e32 v98, 16, v143
	v_and_b32_e32 v99, 0xffff0000, v143
	v_pk_fma_f32 v[108:109], v[100:101], v[108:109], v[98:99]
	v_cvt_pk_bf16_f32 v98, v102, v103
	v_lshl_add_u64 v[102:103], s[4:5], 0, v[208:209]
	v_cvt_pk_bf16_f32 v99, v104, v105
	v_cvt_pk_bf16_f32 v100, v106, v107
	v_cvt_pk_bf16_f32 v101, v108, v109
	v_lshl_add_u64 v[142:143], v[102:103], 0, v[192:193]
	global_store_dwordx4 v[142:143], v[98:101], off
	s_and_b64 vcc, exec, s[8:9]
	v_mov_b32_e32 v139, 0
	v_add_u32_e32 v98, 0x80, v202
	v_ashrrev_i32_e32 v99, 31, v98
	v_lshlrev_b64 v[100:101], 13, v[98:99]
	v_lshl_add_u64 v[144:145], v[206:207], 0, v[100:101]
	global_load_dwordx4 v[134:137], v[144:145], off nt
	v_lshlrev_b64 v[160:161], 12, v[98:99]
	v_mov_b32_e32 v140, 0
	v_mov_b32_e32 v141, 0
	s_cbranch_vccnz .LBB0_913
	v_lshl_add_u64 v[98:99], v[204:205], 0, v[160:161]
	global_load_dwordx4 v[138:141], v[98:99], off
; __device__ __forceinline__ void unpack8(const v4u w, float (&o)[8]) { o[0] = bflo(w.x); o[1] = bfhi(w.x); o[2] = bflo(w.y); o[3] = bfhi(w.y); o[4] = bflo(w.z); o[5] = bfhi(w.z); o[6] = bflo(w.w); o[7] = bfhi(w.w); }
; __device__ __forceinline__ v4u pack8(const float (&o)[8]) { v4u w; w.x = pk2(o[0], o[1]); w.y = pk2(o[2], o[3]); w.z = pk2(o[4], o[5]); w.w = pk2(o[6], o[7]); return w; }
; __device__ __forceinline__ float sigmf(float x) { return __builtin_amdgcn_rcpf(1.f + __expf(-x)); }
;     __device__ __forceinline__ void operator()(const f32x4 (&acc)[2][2][4][2], const pg8::Unit& u, int wr, int wc, int fr, int fq_in) const {
;     ...
;                 for (int m = 0; m < 4; ++m) { const size_t row = (size_t)(row0 + ai * 128 + m * 16);
;                     gw_[m] = *(const v4u*)(Gt + row * (2 * D) + goff + col); pw_[m] = first ? (v4u){0u, 0u, 0u, 0u} : *(const v4u*)(O + row * D + col); }
;                 __builtin_amdgcn_sched_barrier(0);
; #pragma unroll
;                 for (int m = 0; m < 4; ++m) { const size_t row = (size_t)(row0 + ai * 128 + m * 16);
;                     float g0[8], p[8]; unpack8(gw_[m], g0); unpack8(pw_[m], p);
;                     float o[8];
; #pragma unroll
;                     for (int q = 0; q < 4; ++q) { o[q] = p[q] + sigmf(g0[q] + b0[q]) * acc[ai][bj][m][0][q]; o[4 + q] = p[4 + q] + sigmf(g0[4 + q] + b0[4 + q]) * acc[ai][bj][m][1][q]; }
;                     *(v4u*)(O + row * D + col) = pack8(o); }
.LBB0_913:
	v_add_u32_e32 v98, 0x90, v202
	v_ashrrev_i32_e32 v99, 31, v98
	v_lshlrev_b64 v[100:101], 13, v[98:99]
	v_lshl_add_u64 v[146:147], v[206:207], 0, v[100:101]
	global_load_dwordx4 v[130:133], v[146:147], off nt
	v_mov_b32_e32 v104, 0
	s_and_b64 vcc, exec, s[8:9]
	v_lshlrev_b64 v[158:159], 12, v[98:99]
	v_mov_b32_e32 v126, 0
	v_mov_b32_e32 v127, 0
	v_mov_b32_e32 v128, 0
	v_mov_b32_e32 v129, 0
	s_cbranch_vccnz .LBB0_915
	v_lshl_add_u64 v[98:99], v[204:205], 0, v[158:159]
	global_load_dwordx4 v[126:129], v[98:99], off
.LBB0_915:
	v_add_u32_e32 v98, 0xa0, v202
	v_ashrrev_i32_e32 v99, 31, v98
	v_lshlrev_b64 v[100:101], 13, v[98:99]
	v_lshl_add_u64 v[148:149], v[206:207], 0, v[100:101]
	global_load_dwordx4 v[122:125], v[148:149], off nt
	s_and_b64 vcc, exec, s[8:9]
	v_lshlrev_b64 v[154:155], 12, v[98:99]
	v_mov_b32_e32 v105, 0
	v_mov_b32_e32 v106, 0
	v_mov_b32_e32 v107, 0
	s_cbranch_vccnz .LBB0_917
	v_lshl_add_u64 v[98:99], v[204:205], 0, v[154:155]
	global_load_dwordx4 v[104:107], v[98:99], off
.LBB0_917:
	v_add_u32_e32 v98, 0xb0, v202
	v_ashrrev_i32_e32 v99, 31, v98
	v_lshlrev_b64 v[100:101], 13, v[98:99]
	v_lshl_add_u64 v[150:151], v[206:207], 0, v[100:101]
	global_load_dwordx4 v[108:111], v[150:151], off nt
	v_lshlrev_b64 v[152:153], 12, v[98:99]
	v_mov_b32_e32 v98, 0
	s_and_b64 vcc, exec, s[8:9]
	v_mov_b32_e32 v100, 0
	v_mov_b32_e32 v101, 0
	v_mov_b32_e32 v102, 0
	v_mov_b32_e32 v103, 0
	s_cbranch_vccnz .LBB0_919
	v_lshl_add_u64 v[100:101], v[204:205], 0, v[152:153]
	global_load_dwordx4 v[100:103], v[100:101], off
.LBB0_919:
	s_waitcnt vmcnt(3)
	v_lshlrev_b32_e32 v99, 16, v134
	v_lshlrev_b32_e32 v166, 16, v135
	v_and_b32_e32 v167, 0xffff0000, v135
	v_lshlrev_b32_e32 v135, 16, v136
	v_add_f32_e32 v99, v118, v99
	v_and_b32_e32 v134, 0xffff0000, v134
	v_mul_f32_e32 v99, 0xbfb8aa3b, v99
	v_add_f32_e32 v135, v114, v135
	v_exp_f32_e32 v99, v99
	v_mul_f32_e32 v135, 0xbfb8aa3b, v135
	v_add_f32_e32 v134, v119, v134
	v_exp_f32_e32 v135, v135
	v_mul_f32_e32 v134, 0xbfb8aa3b, v134
	v_lshlrev_b32_e32 v168, 16, v137
	v_and_b32_e32 v169, 0xffff0000, v137
	v_exp_f32_e32 v137, v134
	v_add_f32_e32 v99, 1.0, v99
	v_rcp_f32_e32 v134, v99
	v_add_f32_e32 v99, 1.0, v135
	v_and_b32_e32 v162, 0xffff0000, v136
	v_rcp_f32_e32 v136, v99
	v_add_f32_e32 v99, 1.0, v137
	v_rcp_f32_e32 v135, v99
	v_add_f32_e32 v99, v115, v162
	v_mul_f32_e32 v99, 0xbfb8aa3b, v99
	v_exp_f32_e32 v99, v99
	v_lshlrev_b32_e32 v162, 16, v138
	v_and_b32_e32 v163, 0xffff0000, v138
	v_pk_fma_f32 v[94:95], v[94:95], v[134:135], v[162:163]
	v_add_f32_e32 v99, 1.0, v99
	v_rcp_f32_e32 v137, v99
	v_add_f32_e32 v99, v120, v166
	v_mul_f32_e32 v99, 0xbfb8aa3b, v99
	v_exp_f32_e32 v99, v99
	v_lshlrev_b32_e32 v134, 16, v140
	v_and_b32_e32 v135, 0xffff0000, v140
	v_pk_fma_f32 v[134:135], v[90:91], v[136:137], v[134:135]
	v_add_f32_e32 v91, v116, v168
	v_add_f32_e32 v90, 1.0, v99
	v_mul_f32_e32 v91, 0xbfb8aa3b, v91
	v_add_f32_e32 v99, v121, v167
	v_exp_f32_e32 v91, v91
	v_mul_f32_e32 v99, 0xbfb8aa3b, v99
	v_exp_f32_e32 v99, v99
	v_rcp_f32_e32 v90, v90
	v_add_f32_e32 v91, 1.0, v91
	v_rcp_f32_e32 v136, v91
	v_add_f32_e32 v91, 1.0, v99
	v_add_f32_e32 v99, v117, v169
	v_mul_f32_e32 v99, 0xbfb8aa3b, v99
	v_exp_f32_e32 v99, v99
	v_rcp_f32_e32 v91, v91
	v_lshlrev_b32_e32 v138, 16, v139
	v_and_b32_e32 v139, 0xffff0000, v139
	v_add_f32_e32 v99, 1.0, v99
	v_rcp_f32_e32 v137, v99
	v_pk_fma_f32 v[96:97], v[96:97], v[90:91], v[138:139]
	v_lshlrev_b32_e32 v90, 16, v141
	v_and_b32_e32 v91, 0xffff0000, v141
	v_pk_fma_f32 v[136:137], v[92:93], v[136:137], v[90:91]
	v_cvt_pk_bf16_f32 v90, v94, v95
	v_lshl_add_u64 v[94:95], s[4:5], 0, v[160:161]
	v_cvt_pk_bf16_f32 v91, v96, v97
	v_cvt_pk_bf16_f32 v92, v134, v135
	v_cvt_pk_bf16_f32 v93, v136, v137
	v_lshl_add_u64 v[96:97], v[94:95], 0, v[192:193]
	global_store_dwordx4 v[96:97], v[90:93], off
	s_waitcnt vmcnt(3)
	v_lshlrev_b32_e32 v94, 16, v126
	v_and_b32_e32 v95, 0xffff0000, v126
	v_lshlrev_b32_e32 v90, 16, v130
	v_and_b32_e32 v91, 0xffff0000, v130
	v_add_f32_e32 v90, v118, v90
	v_add_f32_e32 v91, v119, v91
	v_mul_f32_e32 v90, 0xbfb8aa3b, v90
	v_mul_f32_e32 v91, 0xbfb8aa3b, v91
	v_exp_f32_e32 v90, v90
	v_exp_f32_e32 v91, v91
	v_lshlrev_b32_e32 v92, 16, v132
	v_and_b32_e32 v93, 0xffff0000, v132
	v_add_f32_e32 v92, v114, v92
	v_add_f32_e32 v93, v115, v93
	v_add_f32_e32 v90, 1.0, v90
	v_mul_f32_e32 v92, 0xbfb8aa3b, v92
	v_add_f32_e32 v91, 1.0, v91
	v_mul_f32_e32 v93, 0xbfb8aa3b, v93
	v_exp_f32_e32 v92, v92
	v_rcp_f32_e32 v90, v90
	v_rcp_f32_e32 v91, v91
	v_exp_f32_e32 v93, v93
	v_add_f32_e32 v92, 1.0, v92
	v_lshlrev_b32_e32 v99, 16, v131
	v_pk_fma_f32 v[86:87], v[86:87], v[90:91], v[94:95]
	v_add_f32_e32 v90, 1.0, v93
	v_rcp_f32_e32 v92, v92
	v_rcp_f32_e32 v93, v90
	v_add_f32_e32 v90, v120, v99
	v_mul_f32_e32 v90, 0xbfb8aa3b, v90
	v_and_b32_e32 v130, 0xffff0000, v131
	v_lshlrev_b32_e32 v131, 16, v133
	v_exp_f32_e32 v94, v90
	v_lshlrev_b32_e32 v90, 16, v128
	v_and_b32_e32 v91, 0xffff0000, v128
	v_pk_fma_f32 v[90:91], v[82:83], v[92:93], v[90:91]
	v_add_f32_e32 v83, v116, v131
	v_mul_f32_e32 v83, 0xbfb8aa3b, v83
	v_add_f32_e32 v92, v121, v130
	v_exp_f32_e32 v83, v83
	v_mul_f32_e32 v92, 0xbfb8aa3b, v92
	v_exp_f32_e32 v93, v92
	v_and_b32_e32 v132, 0xffff0000, v133
	v_add_f32_e32 v83, 1.0, v83
	v_rcp_f32_e32 v92, v83
	v_add_f32_e32 v83, 1.0, v93
	v_add_f32_e32 v93, v117, v132
	v_mul_f32_e32 v93, 0xbfb8aa3b, v93
	v_exp_f32_e32 v93, v93
	v_add_f32_e32 v82, 1.0, v94
	v_rcp_f32_e32 v82, v82
	v_rcp_f32_e32 v83, v83
	v_add_f32_e32 v93, 1.0, v93
	v_rcp_f32_e32 v93, v93
	v_lshlrev_b32_e32 v94, 16, v127
	v_and_b32_e32 v95, 0xffff0000, v127
	v_pk_fma_f32 v[88:89], v[88:89], v[82:83], v[94:95]
	v_lshlrev_b32_e32 v82, 16, v129
	v_and_b32_e32 v83, 0xffff0000, v129
	v_pk_fma_f32 v[92:93], v[84:85], v[92:93], v[82:83]
	v_cvt_pk_bf16_f32 v82, v86, v87
	v_lshl_add_u64 v[86:87], s[4:5], 0, v[158:159]
	v_cvt_pk_bf16_f32 v83, v88, v89
	v_cvt_pk_bf16_f32 v84, v90, v91
	v_cvt_pk_bf16_f32 v85, v92, v93
	v_lshl_add_u64 v[126:127], v[86:87], 0, v[192:193]
	global_store_dwordx4 v[126:127], v[82:85], off
	s_waitcnt vmcnt(3)
; __device__ __forceinline__ void unpack8(const v4u w, float (&o)[8]) { o[0] = bflo(w.x); o[1] = bfhi(w.x); o[2] = bflo(w.y); o[3] = bfhi(w.y); o[4] = bflo(w.z); o[5] = bfhi(w.z); o[6] = bflo(w.w); o[7] = bfhi(w.w); }
; __device__ __forceinline__ v4u pack8(const float (&o)[8]) { v4u w; w.x = pk2(o[0], o[1]); w.y = pk2(o[2], o[3]); w.z = pk2(o[4], o[5]); w.w = pk2(o[6], o[7]); return w; }
; __device__ __forceinline__ float sigmf(float x) { return __builtin_amdgcn_rcpf(1.f + __expf(-x)); }
;     __device__ __forceinline__ void operator()(const f32x4 (&acc)[2][2][4][2], const pg8::Unit& u, int wr, int wc, int fr, int fq_in) const {
;     ...
;             { const f32x4 t0 = *(const f32x4*)(bg + goff + col), t1 = *(const f32x4*)(bg + goff + col + 4);
; #pragma unroll
;               for (int q = 0; q < 4; ++q) { b0[q] = t0[q]; b0[4 + q] = t1[q]; } }
; #pragma unroll
;             for (int ai = 0; ai < 2; ++ai) {
;                 v4u gw_[4], pw_[4];
; #pragma unroll
;                 for (int m = 0; m < 4; ++m) { const size_t row = (size_t)(row0 + ai * 128 + m * 16);
;                     gw_[m] = *(const v4u*)(Gt + row * (2 * D) + goff + col); pw_[m] = first ? (v4u){0u, 0u, 0u, 0u} : *(const v4u*)(O + row * D + col); }
;                 __builtin_amdgcn_sched_barrier(0);
; #pragma unroll
;                 for (int m = 0; m < 4; ++m) { const size_t row = (size_t)(row0 + ai * 128 + m * 16);
;                     float g0[8], p[8]; unpack8(gw_[m], g0); unpack8(pw_[m], p);
;                     float o[8];
; #pragma unroll
;                     for (int q = 0; q < 4; ++q) { o[q] = p[q] + sigmf(g0[q] + b0[q]) * acc[ai][bj][m][0][q]; o[4 + q] = p[4 + q] + sigmf(g0[4 + q] + b0[4 + q]) * acc[ai][bj][m][1][q]; }
;                     *(v4u*)(O + row * D + col) = pack8(o); }
	v_lshlrev_b32_e32 v86, 16, v104
	v_and_b32_e32 v87, 0xffff0000, v104
	v_lshlrev_b32_e32 v82, 16, v122
	v_and_b32_e32 v83, 0xffff0000, v122
	v_add_f32_e32 v82, v118, v82
	v_add_f32_e32 v83, v119, v83
	v_mul_f32_e32 v82, 0xbfb8aa3b, v82
	v_mul_f32_e32 v83, 0xbfb8aa3b, v83
	v_exp_f32_e32 v82, v82
	v_exp_f32_e32 v83, v83
	v_lshlrev_b32_e32 v84, 16, v124
	v_and_b32_e32 v85, 0xffff0000, v124
	v_add_f32_e32 v84, v114, v84
	v_add_f32_e32 v85, v115, v85
	v_add_f32_e32 v82, 1.0, v82
	v_mul_f32_e32 v84, 0xbfb8aa3b, v84
	v_add_f32_e32 v83, 1.0, v83
	v_mul_f32_e32 v85, 0xbfb8aa3b, v85
	v_exp_f32_e32 v84, v84
	v_rcp_f32_e32 v82, v82
	v_rcp_f32_e32 v83, v83
	v_exp_f32_e32 v85, v85
	v_add_f32_e32 v84, 1.0, v84
	v_lshlrev_b32_e32 v88, 16, v123
	v_pk_fma_f32 v[78:79], v[78:79], v[82:83], v[86:87]
	v_add_f32_e32 v82, 1.0, v85
	v_rcp_f32_e32 v84, v84
	v_rcp_f32_e32 v85, v82
	v_add_f32_e32 v82, v120, v88
	v_mul_f32_e32 v82, 0xbfb8aa3b, v82
	v_lshlrev_b32_e32 v90, 16, v125
	v_exp_f32_e32 v86, v82
	v_lshlrev_b32_e32 v82, 16, v106
	v_and_b32_e32 v83, 0xffff0000, v106
	v_and_b32_e32 v89, 0xffff0000, v123
	v_pk_fma_f32 v[82:83], v[74:75], v[84:85], v[82:83]
	v_add_f32_e32 v75, v116, v90
	v_mul_f32_e32 v75, 0xbfb8aa3b, v75
	v_add_f32_e32 v84, v121, v89
	v_exp_f32_e32 v75, v75
	v_mul_f32_e32 v84, 0xbfb8aa3b, v84
	v_exp_f32_e32 v85, v84
	v_and_b32_e32 v91, 0xffff0000, v125
	v_add_f32_e32 v75, 1.0, v75
	v_rcp_f32_e32 v84, v75
	v_add_f32_e32 v75, 1.0, v85
	v_add_f32_e32 v85, v117, v91
	v_mul_f32_e32 v85, 0xbfb8aa3b, v85
	v_exp_f32_e32 v85, v85
	v_add_f32_e32 v74, 1.0, v86
	v_rcp_f32_e32 v74, v74
	v_rcp_f32_e32 v75, v75
	v_add_f32_e32 v85, 1.0, v85
	v_rcp_f32_e32 v85, v85
	v_lshlrev_b32_e32 v86, 16, v105
	v_and_b32_e32 v87, 0xffff0000, v105
	v_pk_fma_f32 v[80:81], v[80:81], v[74:75], v[86:87]
	v_lshlrev_b32_e32 v74, 16, v107
	v_and_b32_e32 v75, 0xffff0000, v107
	v_pk_fma_f32 v[84:85], v[76:77], v[84:85], v[74:75]
	v_cvt_pk_bf16_f32 v74, v78, v79
	v_lshl_add_u64 v[78:79], s[4:5], 0, v[154:155]
	v_cvt_pk_bf16_f32 v75, v80, v81
	v_cvt_pk_bf16_f32 v76, v82, v83
	v_cvt_pk_bf16_f32 v77, v84, v85
	v_lshl_add_u64 v[122:123], v[78:79], 0, v[192:193]
	global_store_dwordx4 v[122:123], v[74:77], off
	s_waitcnt vmcnt(3)
	v_lshlrev_b32_e32 v78, 16, v100
	v_and_b32_e32 v79, 0xffff0000, v100
	v_lshlrev_b32_e32 v74, 16, v108
	v_and_b32_e32 v75, 0xffff0000, v108
	v_add_f32_e32 v74, v118, v74
	v_add_f32_e32 v75, v119, v75
	v_mul_f32_e32 v74, 0xbfb8aa3b, v74
	v_mul_f32_e32 v75, 0xbfb8aa3b, v75
	v_exp_f32_e32 v74, v74
	v_exp_f32_e32 v75, v75
	v_lshlrev_b32_e32 v76, 16, v110
	v_and_b32_e32 v77, 0xffff0000, v110
	v_add_f32_e32 v76, v114, v76
	v_add_f32_e32 v77, v115, v77
	v_add_f32_e32 v74, 1.0, v74
	v_mul_f32_e32 v76, 0xbfb8aa3b, v76
	v_add_f32_e32 v75, 1.0, v75
	v_mul_f32_e32 v77, 0xbfb8aa3b, v77
	v_exp_f32_e32 v76, v76
	v_rcp_f32_e32 v74, v74
	v_rcp_f32_e32 v75, v75
	v_exp_f32_e32 v77, v77
	v_add_f32_e32 v76, 1.0, v76
	v_lshlrev_b32_e32 v80, 16, v109
	v_pk_fma_f32 v[70:71], v[70:71], v[74:75], v[78:79]
	v_add_f32_e32 v74, 1.0, v77
	v_rcp_f32_e32 v76, v76
	v_rcp_f32_e32 v77, v74
	v_add_f32_e32 v74, v120, v80
	v_mul_f32_e32 v74, 0xbfb8aa3b, v74
	v_lshlrev_b32_e32 v82, 16, v111
	v_exp_f32_e32 v78, v74
	v_lshlrev_b32_e32 v74, 16, v102
	v_and_b32_e32 v75, 0xffff0000, v102
	v_and_b32_e32 v81, 0xffff0000, v109
	v_pk_fma_f32 v[74:75], v[66:67], v[76:77], v[74:75]
	v_add_f32_e32 v67, v116, v82
	v_mul_f32_e32 v67, 0xbfb8aa3b, v67
	v_add_f32_e32 v76, v121, v81
	v_exp_f32_e32 v67, v67
	v_mul_f32_e32 v76, 0xbfb8aa3b, v76
	v_exp_f32_e32 v77, v76
	v_and_b32_e32 v83, 0xffff0000, v111
	v_add_f32_e32 v67, 1.0, v67
	v_rcp_f32_e32 v76, v67
	v_add_f32_e32 v67, 1.0, v77
	v_add_f32_e32 v77, v117, v83
	v_mul_f32_e32 v77, 0xbfb8aa3b, v77
	v_exp_f32_e32 v77, v77
	v_add_f32_e32 v66, 1.0, v78
	v_rcp_f32_e32 v66, v66
	v_rcp_f32_e32 v67, v67
	v_add_f32_e32 v77, 1.0, v77
	v_rcp_f32_e32 v77, v77
	v_lshlrev_b32_e32 v78, 16, v101
	v_and_b32_e32 v79, 0xffff0000, v101
	v_pk_fma_f32 v[72:73], v[72:73], v[66:67], v[78:79]
	v_lshlrev_b32_e32 v66, 16, v103
	v_and_b32_e32 v67, 0xffff0000, v103
	v_pk_fma_f32 v[76:77], v[68:69], v[76:77], v[66:67]
	v_cvt_pk_bf16_f32 v66, v70, v71
	v_lshl_add_u64 v[70:71], s[4:5], 0, v[152:153]
	v_cvt_pk_bf16_f32 v67, v72, v73
	v_cvt_pk_bf16_f32 v68, v74, v75
	v_cvt_pk_bf16_f32 v69, v76, v77
	v_lshl_add_u64 v[110:111], v[70:71], 0, v[192:193]
	global_store_dwordx4 v[110:111], v[66:69], off
	global_load_dwordx4 v[66:69], v[190:191], off offset:528
	s_nop 0
	global_load_dwordx4 v[70:73], v[190:191], off offset:512
	global_load_dwordx4 v[106:109], v[194:195], off offset:256 nt
	s_and_b64 vcc, exec, s[8:9]
	v_mov_b32_e32 v99, 0
	v_mov_b32_e32 v100, 0
	v_mov_b32_e32 v101, 0
	s_cbranch_vccnz .LBB0_921
	global_load_dwordx4 v[98:101], v[164:165], off offset:256
.LBB0_921:
	global_load_dwordx4 v[102:105], v[196:197], off offset:256 nt
	v_mov_b32_e32 v80, 0
	s_and_b64 vcc, exec, s[8:9]
	v_mov_b32_e32 v92, 0
	v_mov_b32_e32 v93, 0
	v_mov_b32_e32 v94, 0
	v_mov_b32_e32 v95, 0
	s_cbranch_vccnz .LBB0_923
	global_load_dwordx4 v[92:95], v[156:157], off offset:256
.LBB0_923:
	global_load_dwordx4 v[88:91], v[198:199], off offset:256 nt
	s_and_b64 vcc, exec, s[8:9]
	v_mov_b32_e32 v81, 0
	v_mov_b32_e32 v82, 0
	v_mov_b32_e32 v83, 0
	s_cbranch_vccnz .LBB0_925
	global_load_dwordx4 v[80:83], v[112:113], off offset:256
.LBB0_925:
	global_load_dwordx4 v[84:87], v[200:201], off offset:256 nt
	v_mov_b32_e32 v74, 0
	s_and_b64 vcc, exec, s[8:9]
	v_mov_b32_e32 v76, 0
	v_mov_b32_e32 v77, 0
	v_mov_b32_e32 v78, 0
	v_mov_b32_e32 v79, 0
	s_cbranch_vccnz .LBB0_927
	global_load_dwordx4 v[76:79], v[142:143], off offset:256
; __device__ __forceinline__ void unpack8(const v4u w, float (&o)[8]) { o[0] = bflo(w.x); o[1] = bfhi(w.x); o[2] = bflo(w.y); o[3] = bfhi(w.y); o[4] = bflo(w.z); o[5] = bfhi(w.z); o[6] = bflo(w.w); o[7] = bfhi(w.w); }
; __device__ __forceinline__ v4u pack8(const float (&o)[8]) { v4u w; w.x = pk2(o[0], o[1]); w.y = pk2(o[2], o[3]); w.z = pk2(o[4], o[5]); w.w = pk2(o[6], o[7]); return w; }
; __device__ __forceinline__ float sigmf(float x) { return __builtin_amdgcn_rcpf(1.f + __expf(-x)); }
;     __device__ __forceinline__ void operator()(const f32x4 (&acc)[2][2][4][2], const pg8::Unit& u, int wr, int wc, int fr, int fq_in) const {
;     ...
;                 for (int m = 0; m < 4; ++m) { const size_t row = (size_t)(row0 + ai * 128 + m * 16);
;                     float g0[8], p[8]; unpack8(gw_[m], g0); unpack8(pw_[m], p);
;                     float o[8];
; #pragma unroll
;                     for (int q = 0; q < 4; ++q) { o[q] = p[q] + sigmf(g0[q] + b0[q]) * acc[ai][bj][m][0][q]; o[4 + q] = p[4 + q] + sigmf(g0[4 + q] + b0[4 + q]) * acc[ai][bj][m][1][q]; }
;                     *(v4u*)(O + row * D + col) = pack8(o); }
.LBB0_927:
	s_waitcnt vmcnt(3)
	v_lshlrev_b32_e32 v75, 16, v106
	v_lshlrev_b32_e32 v116, 16, v107
	v_and_b32_e32 v117, 0xffff0000, v107
	v_lshlrev_b32_e32 v107, 16, v108
	v_add_f32_e32 v75, v70, v75
	v_and_b32_e32 v106, 0xffff0000, v106
	v_mul_f32_e32 v75, 0xbfb8aa3b, v75
	v_add_f32_e32 v107, v66, v107
	v_exp_f32_e32 v75, v75
	v_mul_f32_e32 v107, 0xbfb8aa3b, v107
	v_add_f32_e32 v106, v71, v106
	v_exp_f32_e32 v107, v107
	v_mul_f32_e32 v106, 0xbfb8aa3b, v106
	v_lshlrev_b32_e32 v118, 16, v109
	v_and_b32_e32 v119, 0xffff0000, v109
	v_exp_f32_e32 v109, v106
	v_add_f32_e32 v75, 1.0, v75
	v_rcp_f32_e32 v106, v75
	v_add_f32_e32 v75, 1.0, v107
	v_and_b32_e32 v114, 0xffff0000, v108
	v_rcp_f32_e32 v108, v75
	v_add_f32_e32 v75, 1.0, v109
	v_rcp_f32_e32 v107, v75
	v_add_f32_e32 v75, v67, v114
	v_mul_f32_e32 v75, 0xbfb8aa3b, v75
	v_exp_f32_e32 v75, v75
	v_lshlrev_b32_e32 v114, 16, v98
	v_and_b32_e32 v115, 0xffff0000, v98
	v_pk_fma_f32 v[62:63], v[62:63], v[106:107], v[114:115]
	v_add_f32_e32 v75, 1.0, v75
	v_rcp_f32_e32 v109, v75
	v_add_f32_e32 v75, v72, v116
	v_mul_f32_e32 v75, 0xbfb8aa3b, v75
	v_exp_f32_e32 v75, v75
	v_lshlrev_b32_e32 v106, 16, v100
	v_and_b32_e32 v107, 0xffff0000, v100
	v_pk_fma_f32 v[106:107], v[58:59], v[108:109], v[106:107]
	v_add_f32_e32 v59, v68, v118
	v_add_f32_e32 v58, 1.0, v75
	v_mul_f32_e32 v59, 0xbfb8aa3b, v59
	v_add_f32_e32 v75, v73, v117
	v_exp_f32_e32 v59, v59
	v_mul_f32_e32 v75, 0xbfb8aa3b, v75
	v_exp_f32_e32 v75, v75
	v_rcp_f32_e32 v58, v58
	v_add_f32_e32 v59, 1.0, v59
	v_rcp_f32_e32 v98, v59
	v_add_f32_e32 v59, 1.0, v75
	v_add_f32_e32 v75, v69, v119
	v_mul_f32_e32 v75, 0xbfb8aa3b, v75
	v_exp_f32_e32 v75, v75
	v_rcp_f32_e32 v59, v59
	v_lshlrev_b32_e32 v108, 16, v99
	v_and_b32_e32 v109, 0xffff0000, v99
	v_add_f32_e32 v75, 1.0, v75
	v_rcp_f32_e32 v99, v75
	v_pk_fma_f32 v[64:65], v[64:65], v[58:59], v[108:109]
	v_lshlrev_b32_e32 v58, 16, v101
	v_and_b32_e32 v59, 0xffff0000, v101
	v_pk_fma_f32 v[98:99], v[60:61], v[98:99], v[58:59]
	v_cvt_pk_bf16_f32 v58, v62, v63
	v_cvt_pk_bf16_f32 v59, v64, v65
	v_cvt_pk_bf16_f32 v60, v106, v107
	v_cvt_pk_bf16_f32 v61, v98, v99
	global_store_dwordx4 v[164:165], v[58:61], off offset:256
	s_waitcnt vmcnt(3)
	v_lshlrev_b32_e32 v62, 16, v92
	v_and_b32_e32 v63, 0xffff0000, v92
	v_lshlrev_b32_e32 v58, 16, v102
	v_and_b32_e32 v59, 0xffff0000, v102
	v_add_f32_e32 v58, v70, v58
	v_add_f32_e32 v59, v71, v59
	v_mul_f32_e32 v58, 0xbfb8aa3b, v58
	v_mul_f32_e32 v59, 0xbfb8aa3b, v59
	v_exp_f32_e32 v58, v58
	v_exp_f32_e32 v59, v59
	v_lshlrev_b32_e32 v60, 16, v104
	v_and_b32_e32 v61, 0xffff0000, v104
	v_add_f32_e32 v60, v66, v60
	v_add_f32_e32 v61, v67, v61
	v_add_f32_e32 v58, 1.0, v58
	v_mul_f32_e32 v60, 0xbfb8aa3b, v60
	v_add_f32_e32 v59, 1.0, v59
	v_mul_f32_e32 v61, 0xbfb8aa3b, v61
	v_exp_f32_e32 v60, v60
	v_rcp_f32_e32 v58, v58
	v_rcp_f32_e32 v59, v59
	v_exp_f32_e32 v61, v61
	v_add_f32_e32 v60, 1.0, v60
	v_lshlrev_b32_e32 v64, 16, v103
	v_pk_fma_f32 v[54:55], v[54:55], v[58:59], v[62:63]
	v_add_f32_e32 v58, 1.0, v61
	v_rcp_f32_e32 v60, v60
	v_rcp_f32_e32 v61, v58
	v_add_f32_e32 v58, v72, v64
	v_mul_f32_e32 v58, 0xbfb8aa3b, v58
	v_lshlrev_b32_e32 v75, 16, v105
	v_exp_f32_e32 v62, v58
	v_lshlrev_b32_e32 v58, 16, v94
	v_and_b32_e32 v59, 0xffff0000, v94
	v_and_b32_e32 v65, 0xffff0000, v103
	v_pk_fma_f32 v[58:59], v[50:51], v[60:61], v[58:59]
	v_add_f32_e32 v51, v68, v75
	v_mul_f32_e32 v51, 0xbfb8aa3b, v51
	v_add_f32_e32 v60, v73, v65
	v_exp_f32_e32 v51, v51
	v_mul_f32_e32 v60, 0xbfb8aa3b, v60
	v_exp_f32_e32 v61, v60
	v_and_b32_e32 v98, 0xffff0000, v105
	v_add_f32_e32 v51, 1.0, v51
	v_rcp_f32_e32 v60, v51
	v_add_f32_e32 v51, 1.0, v61
	v_add_f32_e32 v61, v69, v98
	v_mul_f32_e32 v61, 0xbfb8aa3b, v61
	v_exp_f32_e32 v61, v61
	v_add_f32_e32 v50, 1.0, v62
	v_rcp_f32_e32 v50, v50
	v_rcp_f32_e32 v51, v51
	v_add_f32_e32 v61, 1.0, v61
	v_rcp_f32_e32 v61, v61
	v_lshlrev_b32_e32 v62, 16, v93
	v_and_b32_e32 v63, 0xffff0000, v93
	v_pk_fma_f32 v[56:57], v[56:57], v[50:51], v[62:63]
	v_lshlrev_b32_e32 v50, 16, v95
	v_and_b32_e32 v51, 0xffff0000, v95
	v_pk_fma_f32 v[60:61], v[52:53], v[60:61], v[50:51]
	v_cvt_pk_bf16_f32 v50, v54, v55
	v_cvt_pk_bf16_f32 v51, v56, v57
	v_cvt_pk_bf16_f32 v52, v58, v59
	v_cvt_pk_bf16_f32 v53, v60, v61
	global_store_dwordx4 v[156:157], v[50:53], off offset:256
	s_waitcnt vmcnt(3)
; __device__ __forceinline__ void unpack8(const v4u w, float (&o)[8]) { o[0] = bflo(w.x); o[1] = bfhi(w.x); o[2] = bflo(w.y); o[3] = bfhi(w.y); o[4] = bflo(w.z); o[5] = bfhi(w.z); o[6] = bflo(w.w); o[7] = bfhi(w.w); }
; __device__ __forceinline__ v4u pack8(const float (&o)[8]) { v4u w; w.x = pk2(o[0], o[1]); w.y = pk2(o[2], o[3]); w.z = pk2(o[4], o[5]); w.w = pk2(o[6], o[7]); return w; }
; __device__ __forceinline__ float sigmf(float x) { return __builtin_amdgcn_rcpf(1.f + __expf(-x)); }
;     __device__ __forceinline__ void operator()(const f32x4 (&acc)[2][2][4][2], const pg8::Unit& u, int wr, int wc, int fr, int fq_in) const {
;     ...
;                 for (int m = 0; m < 4; ++m) { const size_t row = (size_t)(row0 + ai * 128 + m * 16);
;                     gw_[m] = *(const v4u*)(Gt + row * (2 * D) + goff + col); pw_[m] = first ? (v4u){0u, 0u, 0u, 0u} : *(const v4u*)(O + row * D + col); }
;                 __builtin_amdgcn_sched_barrier(0);
; #pragma unroll
;                 for (int m = 0; m < 4; ++m) { const size_t row = (size_t)(row0 + ai * 128 + m * 16);
;                     float g0[8], p[8]; unpack8(gw_[m], g0); unpack8(pw_[m], p);
;                     float o[8];
; #pragma unroll
;                     for (int q = 0; q < 4; ++q) { o[q] = p[q] + sigmf(g0[q] + b0[q]) * acc[ai][bj][m][0][q]; o[4 + q] = p[4 + q] + sigmf(g0[4 + q] + b0[4 + q]) * acc[ai][bj][m][1][q]; }
;                     *(v4u*)(O + row * D + col) = pack8(o); }
	v_lshlrev_b32_e32 v54, 16, v80
	v_and_b32_e32 v55, 0xffff0000, v80
	v_lshlrev_b32_e32 v50, 16, v88
	v_and_b32_e32 v51, 0xffff0000, v88
	v_add_f32_e32 v50, v70, v50
	v_add_f32_e32 v51, v71, v51
	v_mul_f32_e32 v50, 0xbfb8aa3b, v50
	v_mul_f32_e32 v51, 0xbfb8aa3b, v51
	v_exp_f32_e32 v50, v50
	v_exp_f32_e32 v51, v51
	v_lshlrev_b32_e32 v52, 16, v90
	v_and_b32_e32 v53, 0xffff0000, v90
	v_add_f32_e32 v52, v66, v52
	v_add_f32_e32 v53, v67, v53
	v_add_f32_e32 v50, 1.0, v50
	v_mul_f32_e32 v52, 0xbfb8aa3b, v52
	v_add_f32_e32 v51, 1.0, v51
	v_mul_f32_e32 v53, 0xbfb8aa3b, v53
	v_exp_f32_e32 v52, v52
	v_rcp_f32_e32 v50, v50
	v_rcp_f32_e32 v51, v51
	v_exp_f32_e32 v53, v53
	v_add_f32_e32 v52, 1.0, v52
	v_lshlrev_b32_e32 v56, 16, v89
	v_pk_fma_f32 v[46:47], v[46:47], v[50:51], v[54:55]
	v_add_f32_e32 v50, 1.0, v53
	v_rcp_f32_e32 v52, v52
	v_rcp_f32_e32 v53, v50
	v_add_f32_e32 v50, v72, v56
	v_mul_f32_e32 v50, 0xbfb8aa3b, v50
	v_lshlrev_b32_e32 v58, 16, v91
	v_exp_f32_e32 v54, v50
	v_lshlrev_b32_e32 v50, 16, v82
	v_and_b32_e32 v51, 0xffff0000, v82
	v_and_b32_e32 v57, 0xffff0000, v89
	v_pk_fma_f32 v[50:51], v[42:43], v[52:53], v[50:51]
	v_add_f32_e32 v43, v68, v58
	v_mul_f32_e32 v43, 0xbfb8aa3b, v43
	v_add_f32_e32 v52, v73, v57
	v_exp_f32_e32 v43, v43
	v_mul_f32_e32 v52, 0xbfb8aa3b, v52
	v_exp_f32_e32 v53, v52
	v_and_b32_e32 v59, 0xffff0000, v91
	v_add_f32_e32 v43, 1.0, v43
	v_rcp_f32_e32 v52, v43
	v_add_f32_e32 v43, 1.0, v53
	v_add_f32_e32 v53, v69, v59
	v_mul_f32_e32 v53, 0xbfb8aa3b, v53
	v_exp_f32_e32 v53, v53
	v_add_f32_e32 v42, 1.0, v54
	v_rcp_f32_e32 v42, v42
	v_rcp_f32_e32 v43, v43
	v_add_f32_e32 v53, 1.0, v53
	v_rcp_f32_e32 v53, v53
	v_lshlrev_b32_e32 v54, 16, v81
	v_and_b32_e32 v55, 0xffff0000, v81
	v_pk_fma_f32 v[48:49], v[48:49], v[42:43], v[54:55]
	v_lshlrev_b32_e32 v42, 16, v83
	v_and_b32_e32 v43, 0xffff0000, v83
	v_pk_fma_f32 v[52:53], v[44:45], v[52:53], v[42:43]
	v_cvt_pk_bf16_f32 v42, v46, v47
	v_cvt_pk_bf16_f32 v43, v48, v49
	v_cvt_pk_bf16_f32 v44, v50, v51
	v_cvt_pk_bf16_f32 v45, v52, v53
	global_store_dwordx4 v[112:113], v[42:45], off offset:256
	s_waitcnt vmcnt(3)
	v_lshlrev_b32_e32 v46, 16, v76
	v_and_b32_e32 v47, 0xffff0000, v76
	v_lshlrev_b32_e32 v42, 16, v84
	v_and_b32_e32 v43, 0xffff0000, v84
	v_add_f32_e32 v42, v70, v42
	v_add_f32_e32 v43, v71, v43
	v_mul_f32_e32 v42, 0xbfb8aa3b, v42
	v_mul_f32_e32 v43, 0xbfb8aa3b, v43
	v_exp_f32_e32 v42, v42
	v_exp_f32_e32 v43, v43
	v_lshlrev_b32_e32 v44, 16, v86
	v_and_b32_e32 v45, 0xffff0000, v86
	v_add_f32_e32 v44, v66, v44
	v_add_f32_e32 v45, v67, v45
	v_add_f32_e32 v42, 1.0, v42
	v_mul_f32_e32 v44, 0xbfb8aa3b, v44
	v_add_f32_e32 v43, 1.0, v43
	v_mul_f32_e32 v45, 0xbfb8aa3b, v45
	v_exp_f32_e32 v44, v44
	v_rcp_f32_e32 v42, v42
	v_rcp_f32_e32 v43, v43
	v_exp_f32_e32 v45, v45
	v_add_f32_e32 v44, 1.0, v44
	v_lshlrev_b32_e32 v48, 16, v85
	v_pk_fma_f32 v[38:39], v[38:39], v[42:43], v[46:47]
	v_add_f32_e32 v42, 1.0, v45
	v_rcp_f32_e32 v44, v44
	v_rcp_f32_e32 v45, v42
	v_add_f32_e32 v42, v72, v48
	v_mul_f32_e32 v42, 0xbfb8aa3b, v42
	v_lshlrev_b32_e32 v50, 16, v87
	v_exp_f32_e32 v46, v42
	v_lshlrev_b32_e32 v42, 16, v78
	v_and_b32_e32 v43, 0xffff0000, v78
	v_and_b32_e32 v49, 0xffff0000, v85
	v_pk_fma_f32 v[42:43], v[34:35], v[44:45], v[42:43]
	v_add_f32_e32 v35, v68, v50
	v_mul_f32_e32 v35, 0xbfb8aa3b, v35
	v_add_f32_e32 v44, v73, v49
	v_exp_f32_e32 v35, v35
	v_mul_f32_e32 v44, 0xbfb8aa3b, v44
	v_exp_f32_e32 v45, v44
	v_and_b32_e32 v51, 0xffff0000, v87
	v_add_f32_e32 v35, 1.0, v35
	v_rcp_f32_e32 v44, v35
	v_add_f32_e32 v35, 1.0, v45
	v_add_f32_e32 v45, v69, v51
	v_mul_f32_e32 v45, 0xbfb8aa3b, v45
	v_exp_f32_e32 v45, v45
	v_add_f32_e32 v34, 1.0, v46
	v_rcp_f32_e32 v34, v34
	v_rcp_f32_e32 v35, v35
	v_add_f32_e32 v45, 1.0, v45
	v_rcp_f32_e32 v45, v45
	v_lshlrev_b32_e32 v46, 16, v77
	v_and_b32_e32 v47, 0xffff0000, v77
	v_pk_fma_f32 v[40:41], v[40:41], v[34:35], v[46:47]
	v_lshlrev_b32_e32 v34, 16, v79
	v_and_b32_e32 v35, 0xffff0000, v79
	v_pk_fma_f32 v[44:45], v[36:37], v[44:45], v[34:35]
	v_cvt_pk_bf16_f32 v34, v38, v39
	v_cvt_pk_bf16_f32 v35, v40, v41
	v_cvt_pk_bf16_f32 v36, v42, v43
	v_cvt_pk_bf16_f32 v37, v44, v45
	global_store_dwordx4 v[142:143], v[34:37], off offset:256
	global_load_dwordx4 v[58:61], v[144:145], off offset:256 nt
	s_and_b64 vcc, exec, s[8:9]
	v_mov_b32_e32 v75, 0
	v_mov_b32_e32 v76, 0
	v_mov_b32_e32 v77, 0
	s_cbranch_vccnz .LBB0_929
	global_load_dwordx4 v[74:77], v[96:97], off offset:256
.LBB0_929:
	global_load_dwordx4 v[54:57], v[146:147], off offset:256 nt
	v_mov_b32_e32 v38, 0
	s_and_b64 vcc, exec, s[8:9]
	v_mov_b32_e32 v50, 0
	v_mov_b32_e32 v51, 0
	v_mov_b32_e32 v52, 0
	v_mov_b32_e32 v53, 0
	s_cbranch_vccnz .LBB0_931
	global_load_dwordx4 v[50:53], v[126:127], off offset:256
.LBB0_931:
	global_load_dwordx4 v[46:49], v[148:149], off offset:256 nt
	s_and_b64 vcc, exec, s[8:9]
	v_mov_b32_e32 v39, 0
	v_mov_b32_e32 v40, 0
	v_mov_b32_e32 v41, 0
	s_cbranch_vccnz .LBB0_933
	global_load_dwordx4 v[38:41], v[122:123], off offset:256
.LBB0_933:
	global_load_dwordx4 v[42:45], v[150:151], off offset:256 nt
	v_mov_b32_e32 v34, 0
	s_and_b64 vcc, exec, s[8:9]
	v_mov_b32_e32 v35, 0
	v_mov_b32_e32 v36, 0
	v_mov_b32_e32 v37, 0
	s_cbranch_vccnz .LBB0_935
	global_load_dwordx4 v[34:37], v[110:111], off offset:256
